# attention tile loops: cross-half running-max exchange via v_permlane32_swap + v_max3 instead of a ds_bpermute round trip (masked loop, dilated near and far paths)
# speedup vs baseline: 1.0019x; 1.0019x over previous
.LBB0_1654:
	s_or_b64 exec, exec, s[8:9]
	v_cmp_le_u32_e32 vcc, s17, v97
	s_and_saveexec_b64 s[8:9], vcc
	s_cbranch_execz .LBB0_1635
	s_lshl_b32 s10, s16, 14
	s_setprio 1
	v_add3_u32 v2, s10, v93, v92
	v_add3_u32 v174, s10, v94, v92
	v_add3_u32 v175, s10, v95, v92
	v_add3_u32 v176, s10, v96, v92
	ds_read_b128 v[36:39], v2 offset:50048
	ds_read_b128 v[114:117], v174 offset:50048
	ds_read_b128 v[132:135], v175 offset:50048
	ds_read_b128 v[136:139], v176 offset:50048
	ds_read_b32 v177, v112
	ds_read2_b32 v[140:141], v113 offset0:26 offset1:27
	ds_read2_b32 v[142:143], v113 offset0:24 offset1:25
	ds_read2_b32 v[144:145], v113 offset0:18 offset1:19
	ds_read2_b32 v[146:147], v113 offset0:16 offset1:17
	ds_read2_b32 v[148:149], v113 offset0:10 offset1:11
	ds_read2_b32 v[150:151], v113 offset0:8 offset1:9
	ds_read2_b32 v[152:153], v113 offset0:2 offset1:3
	ds_read2_b32 v[154:155], v113 offset1:1
	s_waitcnt lgkmcnt(12)
	v_mfma_f32_32x32x16_bf16 v[36:51], v[36:39], v[52:55], 0
	s_waitcnt lgkmcnt(11)
	v_mfma_f32_32x32x16_bf16 v[36:51], v[114:117], v[56:59], v[36:51]
	s_waitcnt lgkmcnt(10)
	v_mfma_f32_32x32x16_bf16 v[36:51], v[132:135], v[60:63], v[36:51]
	s_waitcnt lgkmcnt(9)
	v_mfma_f32_32x32x16_bf16 v[36:51], v[136:139], v[64:67], v[36:51]
	s_setprio 0
	v_add3_u32 v174, s10, v98, v107
	v_add3_u32 v175, s10, v99, v107
	ds_read_b128 v[156:159], v174 offset:58240
	ds_read_b128 v[162:165], v174 offset:60288
	ds_read_b128 v[166:169], v175 offset:58240
	ds_read_b128 v[170:173], v175 offset:60288
	s_waitcnt lgkmcnt(4)
	v_lshrrev_b32_e32 v2, v102, v177
	v_bfe_i32 v178, v2, 0, 1
	v_bfe_i32 v179, v2, 1, 1
	v_bfe_i32 v180, v2, 2, 1
	v_bfe_i32 v181, v2, 3, 1
	v_bfe_i32 v182, v2, 8, 1
	v_bfe_i32 v183, v2, 9, 1
	v_bfe_i32 v184, v2, 10, 1
	v_bfe_i32 v185, v2, 11, 1
	v_bfe_i32 v186, v2, 16, 1
	v_bfe_i32 v187, v2, 17, 1
	v_bfe_i32 v188, v2, 18, 1
	v_bfe_i32 v189, v2, 19, 1
	v_bfe_i32 v190, v2, 24, 1
	v_bfe_i32 v191, v2, 25, 1
	v_bfe_i32 v192, v2, 26, 1
	v_bfe_i32 v193, v2, 27, 1
	v_pk_fma_f32 v[36:37], v[36:37], s[82:83], v[140:141] op_sel:[0,0,1] op_sel_hi:[1,0,0]
	v_pk_fma_f32 v[38:39], v[38:39], s[82:83], v[142:143] op_sel:[0,0,1] op_sel_hi:[1,0,0]
	v_bfi_b32 v36, v178, v36, v228
	v_bfi_b32 v37, v179, v37, v228
	v_bfi_b32 v38, v180, v38, v228
	v_bfi_b32 v39, v181, v39, v228
	v_max_f32_e32 v116, v36, v37
	v_max_f32_e32 v114, v38, v39
	v_max3_f32 v116, v116, s90, v114
	v_pk_fma_f32 v[40:41], v[40:41], s[82:83], v[144:145] op_sel:[0,0,1] op_sel_hi:[1,0,0]
	v_pk_fma_f32 v[42:43], v[42:43], s[82:83], v[146:147] op_sel:[0,0,1] op_sel_hi:[1,0,0]
	v_bfi_b32 v40, v182, v40, v228
	v_bfi_b32 v41, v183, v41, v228
	v_bfi_b32 v42, v184, v42, v228
	v_bfi_b32 v43, v185, v43, v228
	v_max_f32_e32 v117, v40, v41
	v_max_f32_e32 v114, v42, v43
	v_max3_f32 v116, v116, v117, v114
	v_pk_fma_f32 v[44:45], v[44:45], s[82:83], v[148:149] op_sel:[0,0,1] op_sel_hi:[1,0,0]
	v_pk_fma_f32 v[46:47], v[46:47], s[82:83], v[150:151] op_sel:[0,0,1] op_sel_hi:[1,0,0]
	v_bfi_b32 v44, v186, v44, v228
	v_bfi_b32 v45, v187, v45, v228
	v_bfi_b32 v46, v188, v46, v228
	v_bfi_b32 v47, v189, v47, v228
	v_max_f32_e32 v117, v44, v45
	v_max_f32_e32 v114, v46, v47
	v_max3_f32 v116, v116, v117, v114
	v_pk_fma_f32 v[48:49], v[48:49], s[82:83], v[152:153] op_sel:[0,0,1] op_sel_hi:[1,0,0]
	v_pk_fma_f32 v[50:51], v[50:51], s[82:83], v[154:155] op_sel:[0,0,1] op_sel_hi:[1,0,0]
	v_bfi_b32 v48, v190, v48, v228
	v_bfi_b32 v49, v191, v49, v228
	v_bfi_b32 v50, v192, v50, v228
	v_bfi_b32 v51, v193, v51, v228
	v_max_f32_e32 v117, v48, v49
	v_max_f32_e32 v2, v50, v51
	v_max3_f32 v2, v116, v117, v2
	v_mov_b32_e32 v114, v2
	v_mov_b32_e32 v115, v2
	s_nop 1
	v_permlane32_swap_b32_e32 v114, v115
	v_max3_f32 v2, v2, v114, v115
	v_add_f32_e32 v114, 0x41000000, v90
	v_cmp_gt_f32_e32 vcc, v2, v114
	s_cbranch_vccz .LBB0_1634
	v_max_f32_e32 v2, v2, v2
	v_max_f32_e32 v114, v90, v90
	v_max_f32_e32 v114, v114, v2
	v_sub_f32_e32 v2, v90, v114
	v_exp_f32_e32 v2, v2
	v_mov_b32_e32 v90, v114
	v_pk_mul_f32 v[34:35], v[34:35], v[2:3] op_sel_hi:[1,0]
	v_pk_mul_f32 v[32:33], v[32:33], v[2:3] op_sel_hi:[1,0]
	v_pk_mul_f32 v[30:31], v[30:31], v[2:3] op_sel_hi:[1,0]
	v_pk_mul_f32 v[28:29], v[28:29], v[2:3] op_sel_hi:[1,0]
	v_pk_mul_f32 v[26:27], v[26:27], v[2:3] op_sel_hi:[1,0]
	v_pk_mul_f32 v[24:25], v[24:25], v[2:3] op_sel_hi:[1,0]
	v_pk_mul_f32 v[22:23], v[22:23], v[2:3] op_sel_hi:[1,0]
	v_pk_mul_f32 v[20:21], v[20:21], v[2:3] op_sel_hi:[1,0]
	v_pk_mul_f32 v[18:19], v[18:19], v[2:3] op_sel_hi:[1,0]
	v_pk_mul_f32 v[16:17], v[16:17], v[2:3] op_sel_hi:[1,0]
	v_pk_mul_f32 v[14:15], v[14:15], v[2:3] op_sel_hi:[1,0]
	v_pk_mul_f32 v[12:13], v[12:13], v[2:3] op_sel_hi:[1,0]
	v_pk_mul_f32 v[10:11], v[10:11], v[2:3] op_sel_hi:[1,0]
	v_pk_mul_f32 v[8:9], v[8:9], v[2:3] op_sel_hi:[1,0]
	v_pk_mul_f32 v[6:7], v[6:7], v[2:3] op_sel_hi:[1,0]
	v_pk_mul_f32 v[4:5], v[4:5], v[2:3] op_sel_hi:[1,0]
	v_mul_f32_e32 v110, v110, v2
	s_branch .LBB0_1634

.LBB0_1709:
	s_or_b64 exec, exec, s[34:35]
	v_cmp_le_u32_e32 vcc, s49, v144
	s_and_saveexec_b64 s[34:35], vcc
	s_cbranch_execz .LBB0_1690
	s_lshl_b32 s36, s46, 14
	s_add_i32 s38, s36, 0
	s_setprio 1
	v_add3_u32 v2, s38, v140, v139
	v_add3_u32 v202, s38, v141, v139
	v_add3_u32 v203, s38, v142, v139
	v_add3_u32 v204, s38, v143, v139
	ds_read_b128 v[36:39], v2 offset:16640
	ds_read_b128 v[52:55], v202 offset:16640
	ds_read_b128 v[178:181], v203 offset:16640
	ds_read_b128 v[182:185], v204 offset:16640
	v_add3_u32 v202, s38, v145, v152
	v_add3_u32 v203, s38, v146, v152
	ds_read_b128 v[186:189], v202 offset:24832
	ds_read_b128 v[190:193], v202 offset:26880
	ds_read_b128 v[194:197], v203 offset:24832
	ds_read_b128 v[198:201], v203 offset:26880
	s_waitcnt lgkmcnt(7)
	v_mfma_f32_32x32x16_bf16 v[36:51], v[36:39], v[92:95], 0
	s_waitcnt lgkmcnt(6)
	v_mfma_f32_32x32x16_bf16 v[36:51], v[52:55], v[96:99], v[36:51]
	s_waitcnt lgkmcnt(5)
	v_mfma_f32_32x32x16_bf16 v[36:51], v[178:181], v[100:103], v[36:51]
	s_waitcnt lgkmcnt(4)
	v_mfma_f32_32x32x16_bf16 v[36:51], v[182:185], v[104:107], v[36:51]
	s_setprio 0
	s_mov_b64 s[36:37], -1
	s_cmp_ge_i32 s47, s42
	v_add_f32_e32 v159, 0x41000000, v158
	s_cbranch_scc0 .LBB0_1714
	v_add_u32_e32 v2, 0x1e7c, v156
	v_add_u32_e32 v205, 0x1e74, v156
	v_add_u32_e32 v56, 0x1e5c, v156
	v_add_u32_e32 v58, 0x1e54, v156
	ds_read2_b32 v[52:53], v2 offset1:1
	ds_read2_b32 v[54:55], v205 offset1:1
	ds_read2_b32 v[56:57], v56 offset1:1
	ds_read2_b32 v[58:59], v58 offset1:1
	v_add_u32_e32 v2, 0x1e3c, v156
	v_add_u32_e32 v205, 0x1e34, v156
	v_add_u32_e32 v235, 0x1e1c, v156
	v_add_u32_e32 v236, 0x1e14, v156
	ds_read2_b32 v[206:207], v2 offset1:1
	ds_read2_b32 v[208:209], v205 offset1:1
	ds_read2_b32 v[210:211], v235 offset1:1
	ds_read2_b32 v[212:213], v236 offset1:1
	s_waitcnt lgkmcnt(4)
	v_pk_fma_f32 v[130:131], v[36:37], s[82:83], v[52:53] op_sel:[0,0,1] op_sel_hi:[1,0,0]
	v_pk_fma_f32 v[88:89], v[38:39], s[82:83], v[54:55] op_sel:[0,0,1] op_sel_hi:[1,0,0]
	v_max_f32_e32 v2, v130, v131
	v_max_f32_e32 v52, v88, v89
	v_pk_fma_f32 v[86:87], v[40:41], s[82:83], v[56:57] op_sel:[0,0,1] op_sel_hi:[1,0,0]
	v_pk_fma_f32 v[84:85], v[42:43], s[82:83], v[58:59] op_sel:[0,0,1] op_sel_hi:[1,0,0]
	v_max3_f32 v2, v2, s90, v52
	v_max_f32_e32 v52, v86, v87
	v_max_f32_e32 v53, v84, v85
	v_max3_f32 v2, v2, v52, v53
	s_waitcnt lgkmcnt(0)
	v_pk_fma_f32 v[136:137], v[44:45], s[82:83], v[206:207] op_sel:[0,0,1] op_sel_hi:[1,0,0]
	v_mov_b32_e32 v160, v157
	v_pk_fma_f32 v[134:135], v[46:47], s[82:83], v[208:209] op_sel:[0,0,1] op_sel_hi:[1,0,0]
	v_max_f32_e32 v52, v136, v137
	v_max_f32_e32 v53, v134, v135
	v_pk_fma_f32 v[132:133], v[48:49], s[82:83], v[210:211] op_sel:[0,0,1] op_sel_hi:[1,0,0]
	v_pk_fma_f32 v[90:91], v[50:51], s[82:83], v[212:213] op_sel:[0,0,1] op_sel_hi:[1,0,0]
	v_max3_f32 v2, v2, v52, v53
	v_max_f32_e32 v52, v132, v133
	v_max_f32_e32 v53, v90, v91
	v_max3_f32 v2, v2, v52, v53
	v_mov_b32_e32 v52, v2
	v_mov_b32_e32 v53, v2
	s_nop 1
	v_permlane32_swap_b32_e32 v52, v53
	v_max3_f32 v161, v2, v52, v53
	v_cmp_gt_f32_e32 vcc, v161, v159
	v_mov_b32_e32 v2, v158
	s_cbranch_vccz .LBB0_1713
	v_max_f32_e32 v2, v161, v161
	v_max_f32_e32 v52, v158, v158
	v_max_f32_e32 v2, v52, v2
	v_sub_f32_e32 v52, v158, v2
	v_exp_f32_e32 v160, v52
	s_nop 0
	v_pk_mul_f32 v[34:35], v[34:35], v[160:161] op_sel_hi:[1,0]
	v_pk_mul_f32 v[32:33], v[32:33], v[160:161] op_sel_hi:[1,0]
	v_pk_mul_f32 v[30:31], v[30:31], v[160:161] op_sel_hi:[1,0]
	v_pk_mul_f32 v[28:29], v[28:29], v[160:161] op_sel_hi:[1,0]
	v_pk_mul_f32 v[26:27], v[26:27], v[160:161] op_sel_hi:[1,0]
	v_pk_mul_f32 v[24:25], v[24:25], v[160:161] op_sel_hi:[1,0]
	v_pk_mul_f32 v[22:23], v[22:23], v[160:161] op_sel_hi:[1,0]
	v_pk_mul_f32 v[20:21], v[20:21], v[160:161] op_sel_hi:[1,0]
	v_pk_mul_f32 v[18:19], v[18:19], v[160:161] op_sel_hi:[1,0]
	v_pk_mul_f32 v[16:17], v[16:17], v[160:161] op_sel_hi:[1,0]
	v_pk_mul_f32 v[14:15], v[14:15], v[160:161] op_sel_hi:[1,0]
	v_pk_mul_f32 v[12:13], v[12:13], v[160:161] op_sel_hi:[1,0]
	v_pk_mul_f32 v[10:11], v[10:11], v[160:161] op_sel_hi:[1,0]
	v_pk_mul_f32 v[8:9], v[8:9], v[160:161] op_sel_hi:[1,0]
	v_pk_mul_f32 v[6:7], v[6:7], v[160:161] op_sel_hi:[1,0]
	v_pk_mul_f32 v[4:5], v[4:5], v[160:161] op_sel_hi:[1,0]
	v_mul_f32_e32 v160, v157, v160

.LBB0_1719:
	s_or_b64 exec, exec, s[36:37]
	v_max_f32_e32 v36, v2, v2
	v_max_f32_e32 v37, v52, v52
	v_max_f32_e32 v36, v37, v36
	v_mov_b32_e32 v37, v36
	v_mov_b32_e32 v38, v36
	s_nop 1
	v_permlane32_swap_b32_e32 v37, v38
	v_max3_f32 v36, v36, v37, v38
	v_cmp_gt_f32_e32 vcc, v36, v159
	s_cbranch_vccz .LBB0_1688
	v_max_f32_e32 v36, v36, v36
	v_max_f32_e32 v37, v158, v158
	v_max_f32_e32 v37, v37, v36
	v_sub_f32_e32 v36, v158, v37
	v_exp_f32_e32 v36, v36
	v_mov_b32_e32 v158, v37
	v_pk_mul_f32 v[34:35], v[34:35], v[36:37] op_sel_hi:[1,0]
	v_pk_mul_f32 v[32:33], v[32:33], v[36:37] op_sel_hi:[1,0]
	v_pk_mul_f32 v[30:31], v[30:31], v[36:37] op_sel_hi:[1,0]
	v_pk_mul_f32 v[28:29], v[28:29], v[36:37] op_sel_hi:[1,0]
	v_pk_mul_f32 v[26:27], v[26:27], v[36:37] op_sel_hi:[1,0]
	v_pk_mul_f32 v[24:25], v[24:25], v[36:37] op_sel_hi:[1,0]
	v_pk_mul_f32 v[22:23], v[22:23], v[36:37] op_sel_hi:[1,0]
	v_pk_mul_f32 v[20:21], v[20:21], v[36:37] op_sel_hi:[1,0]
	v_pk_mul_f32 v[18:19], v[18:19], v[36:37] op_sel_hi:[1,0]
	v_pk_mul_f32 v[16:17], v[16:17], v[36:37] op_sel_hi:[1,0]
	v_pk_mul_f32 v[14:15], v[14:15], v[36:37] op_sel_hi:[1,0]
	v_pk_mul_f32 v[12:13], v[12:13], v[36:37] op_sel_hi:[1,0]
	v_pk_mul_f32 v[10:11], v[10:11], v[36:37] op_sel_hi:[1,0]
	v_pk_mul_f32 v[8:9], v[8:9], v[36:37] op_sel_hi:[1,0]
	v_pk_mul_f32 v[6:7], v[6:7], v[36:37] op_sel_hi:[1,0]
	v_pk_mul_f32 v[4:5], v[4:5], v[36:37] op_sel_hi:[1,0]
	v_mul_f32_e32 v157, v157, v36
	s_branch .LBB0_1688
